# waits to first consumer without extra instructions: next group's 3rd/4th V-fragment reads issued two MFMAs earlier into a second register pair (alternating per group), so each P.V transition wait has
# speedup vs baseline: 1.0146x; 1.0146x over previous
.LBB0_787:
	ds_read_b128 v[80:83], v134 offset:33792
	ds_read_b128 v[84:87], v134 offset:41984
	ds_read_b128 v[196:199], v135 offset:33792
	ds_read_b128 v[200:203], v135 offset:41984
	s_waitcnt lgkmcnt(2)
	v_mfma_f32_32x32x16_bf16 v[96:111], v[80:83], v[122:125], 0
	v_exp_f32_e32 v204, v72
	v_exp_f32_e32 v205, v73
	v_exp_f32_e32 v206, v74
	v_exp_f32_e32 v207, v75
	v_exp_f32_e32 v208, v76
	v_exp_f32_e32 v209, v77
	v_mfma_f32_32x32x16_bf16 v[80:95], v[84:87], v[122:125], 0
	v_exp_f32_e32 v210, v78
	v_exp_f32_e32 v79, v79
	s_waitcnt lgkmcnt(0)
	v_mfma_f32_32x32x16_bf16 v[96:111], v[196:199], v[126:129], v[96:111]
	v_mfma_f32_32x32x16_bf16 v[80:95], v[200:203], v[126:129], v[80:95]
	ds_read_b128 v[196:199], v136 offset:33792
	ds_read_b128 v[200:203], v136 offset:41984
	s_waitcnt lgkmcnt(0)
	v_mfma_f32_32x32x16_bf16 v[96:111], v[196:199], v[118:121], v[96:111]
	v_mfma_f32_32x32x16_bf16 v[80:95], v[200:203], v[118:121], v[80:95]
	ds_read_b128 v[196:199], v137 offset:33792
	ds_read_b128 v[200:203], v137 offset:41984
	v_exp_f32_e32 v180, v64
	v_add_f32_e32 v64, v161, v159
	v_add_f32_e32 v195, v157, v160
	v_add_f32_e32 v64, v155, v64
	v_add_f32_e32 v195, v158, v195
	v_add_f32_e32 v64, v154, v64
	v_add_f32_e32 v195, v156, v195
	v_add_f32_e32 v64, v151, v64
	v_add_f32_e32 v195, v153, v195
	v_add_f32_e32 v64, v149, v64
	v_add_f32_e32 v195, v152, v195
	v_add_f32_e32 v64, v147, v64
	s_waitcnt lgkmcnt(0)
	v_mfma_f32_32x32x16_bf16 v[96:111], v[196:199], v[114:117], v[96:111]
	v_exp_f32_e32 v197, v65
	v_add_f32_e32 v195, v150, v195
	v_exp_f32_e32 v198, v66
	v_add_f32_e32 v64, v146, v64
	v_exp_f32_e32 v199, v67
	v_add_f32_e32 v195, v148, v195
	v_add_f32_e32 v64, v180, v64
	v_mfma_f32_32x32x16_bf16 v[80:95], v[200:203], v[114:117], v[80:95]
	v_exp_f32_e32 v200, v68
	v_exp_f32_e32 v201, v69
	v_add_f32_e32 v195, v197, v195
	v_exp_f32_e32 v202, v70
	v_add_f32_e32 v64, v198, v64
	v_exp_f32_e32 v203, v71
	v_add_f32_e32 v195, v199, v195
	v_add_f32_e32 v64, v200, v64
	v_add_f32_e32 v195, v201, v195
	v_add_f32_e32 v64, v202, v64
	v_add_f32_e32 v195, v203, v195
	v_add_f32_e32 v64, v204, v64
	v_add_f32_e32 v195, v205, v195
	v_add_f32_e32 v64, v206, v64
	v_add_f32_e32 v195, v207, v195
	v_add_f32_e32 v64, v208, v64
	v_add_f32_e32 v195, v209, v195
	v_add_f32_e32 v64, v210, v64
	v_add_f32_e32 v195, v79, v195
	v_add_f32_e32 v195, v195, v64
	v_cvt_pk_bf16_f32 v64, v159, v161
	v_cvt_pk_bf16_f32 v65, v157, v160
	v_cvt_pk_bf16_f32 v66, v155, v158
	v_cvt_pk_bf16_f32 v67, v154, v156
	v_cvt_pk_bf16_f32 v68, v151, v153
	v_cvt_pk_bf16_f32 v69, v149, v152
	v_cvt_pk_bf16_f32 v70, v147, v150
	v_cvt_pk_bf16_f32 v71, v146, v148
	v_cvt_pk_bf16_f32 v72, v180, v197
	v_cvt_pk_bf16_f32 v73, v198, v199
	v_cvt_pk_bf16_f32 v74, v200, v201
	v_cvt_pk_bf16_f32 v75, v202, v203
	v_cvt_pk_bf16_f32 v76, v204, v205
	v_cvt_pk_bf16_f32 v77, v206, v207
	v_cvt_pk_bf16_f32 v78, v208, v209
	v_cvt_pk_bf16_f32 v79, v210, v79
	s_add_i32 m0, s84, 0x8400
	s_add_u32 s66, s78, s65
	s_addc_u32 s67, s79, 0
	global_load_lds_dwordx4 v185, s[66:67]
	s_add_i32 m0, s84, 0xa400
	s_add_i32 s64, s65, 0x60000
	global_load_lds_dwordx4 v184, s[66:67]
	s_add_i32 m0, s84, 0xc400
	s_add_u32 s70, s80, s64
	s_addc_u32 s71, s81, 0
	global_load_lds_dwordx4 v183, s[70:71]
	s_add_i32 m0, s84, 0xe400
	s_mov_b32 s65, s64
	global_load_lds_dwordx4 v182, s[70:71]
	ds_read_b64_tr_b16 v[198:199], v192 offset:1024
	ds_read_b64_tr_b16 v[200:201], v192 offset:3072
	ds_read_b64_tr_b16 v[202:203], v192 offset:5120
	ds_read_b64_tr_b16 v[204:205], v192 offset:7168
	ds_read_b64_tr_b16 v[206:207], v192 offset:9216
	ds_read_b64_tr_b16 v[208:209], v192 offset:11264
	ds_read_b64_tr_b16 v[222:223], v192 offset:13312
	ds_read_b64_tr_b16 v[224:225], v192 offset:15360
	s_waitcnt lgkmcnt(0)
	v_mfma_f32_32x32x16_bf16 v[0:15], v[64:67], v[198:201], v[0:15]
	ds_read_b64_tr_b16 v[198:199], v192 offset:1536
	ds_read_b64_tr_b16 v[200:201], v192 offset:3584
	ds_read_b64_tr_b16 v[138:139], v192 offset:9728
	ds_read_b64_tr_b16 v[140:141], v192 offset:11776
	v_mfma_f32_32x32x16_bf16 v[0:15], v[68:71], v[202:205], v[0:15]
	ds_read_b64_tr_b16 v[202:203], v192 offset:5632
	ds_read_b64_tr_b16 v[204:205], v192 offset:7680
	ds_read_b64_tr_b16 v[142:143], v192 offset:13824
	ds_read_b64_tr_b16 v[144:145], v192 offset:15872
	v_mfma_f32_32x32x16_bf16 v[0:15], v[72:75], v[206:209], v[0:15]
	v_mfma_f32_32x32x16_bf16 v[0:15], v[76:79], v[222:225], v[0:15]
	s_waitcnt lgkmcnt(0)
	v_mfma_f32_32x32x16_bf16 v[48:63], v[64:67], v[198:201], v[48:63]
	ds_read_b64_tr_b16 v[198:199], v192 offset:2048
	ds_read_b64_tr_b16 v[200:201], v192 offset:4096
	ds_read_b64_tr_b16 v[206:207], v192 offset:10240
	ds_read_b64_tr_b16 v[208:209], v192 offset:12288
	v_mfma_f32_32x32x16_bf16 v[48:63], v[68:71], v[202:205], v[48:63]
	ds_read_b64_tr_b16 v[202:203], v192 offset:6144
	ds_read_b64_tr_b16 v[204:205], v192 offset:8192
	ds_read_b64_tr_b16 v[222:223], v192 offset:14336
	ds_read_b64_tr_b16 v[224:225], v192 offset:16384
	v_mfma_f32_32x32x16_bf16 v[48:63], v[72:75], v[138:141], v[48:63]
	v_mfma_f32_32x32x16_bf16 v[48:63], v[76:79], v[142:145], v[48:63]
	s_waitcnt lgkmcnt(0)
	v_mfma_f32_32x32x16_bf16 v[32:47], v[64:67], v[198:201], v[32:47]
	ds_read_b64_tr_b16 v[198:199], v192 offset:2560
	ds_read_b64_tr_b16 v[200:201], v192 offset:4608
	ds_read_b64_tr_b16 v[138:139], v192 offset:10752
	ds_read_b64_tr_b16 v[140:141], v192 offset:12800
	v_mfma_f32_32x32x16_bf16 v[32:47], v[68:71], v[202:205], v[32:47]
	ds_read_b64_tr_b16 v[202:203], v192 offset:6656
	ds_read_b64_tr_b16 v[204:205], v192 offset:8704
	ds_read_b64_tr_b16 v[142:143], v192 offset:14848
	ds_read_b64_tr_b16 v[144:145], v192 offset:16896
	v_mfma_f32_32x32x16_bf16 v[32:47], v[72:75], v[206:209], v[32:47]
	v_mfma_f32_32x32x16_bf16 v[32:47], v[76:79], v[222:225], v[32:47]
	s_waitcnt lgkmcnt(0)
	v_mfma_f32_32x32x16_bf16 v[16:31], v[64:67], v[198:201], v[16:31]
	v_max_f32_e32 v64, v96, v97
	v_max3_f32 v65, v80, v81, v82
	v_max3_f32 v64, v64, v98, v99
	v_max3_f32 v65, v65, v83, v84
	v_max3_f32 v64, v64, v100, v101
	v_mfma_f32_32x32x16_bf16 v[16:31], v[68:71], v[202:205], v[16:31]
	v_max3_f32 v65, v65, v85, v86
	v_max3_f32 v64, v64, v102, v103
	v_max3_f32 v65, v65, v87, v88
	v_max3_f32 v64, v64, v104, v105
	v_max3_f32 v65, v65, v89, v90
	v_max3_f32 v64, v64, v106, v107
	v_max3_f32 v65, v65, v91, v92
	v_mfma_f32_32x32x16_bf16 v[16:31], v[72:75], v[138:141], v[16:31]
	v_max3_f32 v64, v64, v108, v109
	v_max3_f32 v65, v65, v93, v94
	v_max3_f32 v64, v64, v110, v111
	v_max3_f32 v64, v64, v65, v95
	v_mov_b32_e32 v198, 1.0
	v_mfma_f32_32x32x16_bf16 v[16:31], v[76:79], v[142:145], v[16:31]
	v_cmp_ge_f32_e64 s[0:1], s56, v64
	s_cmp_eq_u64 s[0:1], exec
	s_cbranch_scc1 .LBB0_792
	s_branch .LBB0_801

.LBB0_794:
	ds_read_b64_tr_b16 v[202:203], v192 offset:17408
	ds_read_b64_tr_b16 v[204:205], v192 offset:19456
	ds_read_b64_tr_b16 v[206:207], v192 offset:21504
	ds_read_b64_tr_b16 v[208:209], v192 offset:23552
	ds_read_b64_tr_b16 v[222:223], v192 offset:25600
	ds_read_b64_tr_b16 v[224:225], v192 offset:27648
	ds_read_b64_tr_b16 v[226:227], v192 offset:29696
	ds_read_b64_tr_b16 v[228:229], v192 offset:31744
	s_waitcnt lgkmcnt(0)
	v_mfma_f32_32x32x16_bf16 v[0:15], v[80:83], v[202:205], v[0:15]
	ds_read_b64_tr_b16 v[202:203], v192 offset:17920
	ds_read_b64_tr_b16 v[204:205], v192 offset:19968
	ds_read_b64_tr_b16 v[138:139], v192 offset:26112
	ds_read_b64_tr_b16 v[140:141], v192 offset:28160
	v_mfma_f32_32x32x16_bf16 v[0:15], v[84:87], v[206:209], v[0:15]
	ds_read_b64_tr_b16 v[206:207], v192 offset:22016
	ds_read_b64_tr_b16 v[208:209], v192 offset:24064
	ds_read_b64_tr_b16 v[142:143], v192 offset:30208
	ds_read_b64_tr_b16 v[144:145], v192 offset:32256
	v_mfma_f32_32x32x16_bf16 v[0:15], v[88:91], v[222:225], v[0:15]
	v_mfma_f32_32x32x16_bf16 v[0:15], v[92:95], v[226:229], v[0:15]
	s_waitcnt lgkmcnt(0)
	v_mfma_f32_32x32x16_bf16 v[48:63], v[80:83], v[202:205], v[48:63]
	ds_read_b64_tr_b16 v[202:203], v192 offset:18432
	ds_read_b64_tr_b16 v[204:205], v192 offset:20480
	ds_read_b64_tr_b16 v[222:223], v192 offset:26624
	ds_read_b64_tr_b16 v[224:225], v192 offset:28672
	v_mfma_f32_32x32x16_bf16 v[48:63], v[84:87], v[206:209], v[48:63]
	ds_read_b64_tr_b16 v[206:207], v192 offset:22528
	ds_read_b64_tr_b16 v[208:209], v192 offset:24576
	ds_read_b64_tr_b16 v[226:227], v192 offset:30720
	ds_read_b64_tr_b16 v[228:229], v192 offset:32768
	v_mfma_f32_32x32x16_bf16 v[48:63], v[88:91], v[138:141], v[48:63]
	v_mfma_f32_32x32x16_bf16 v[48:63], v[92:95], v[142:145], v[48:63]
	s_waitcnt lgkmcnt(0)
	v_mfma_f32_32x32x16_bf16 v[32:47], v[80:83], v[202:205], v[32:47]
	ds_read_b64_tr_b16 v[202:203], v192 offset:18944
	ds_read_b64_tr_b16 v[204:205], v192 offset:20992
	ds_read_b64_tr_b16 v[138:139], v192 offset:27136
	ds_read_b64_tr_b16 v[140:141], v192 offset:29184
	v_mfma_f32_32x32x16_bf16 v[32:47], v[84:87], v[206:209], v[32:47]
	ds_read_b64_tr_b16 v[206:207], v192 offset:23040
	ds_read_b64_tr_b16 v[208:209], v192 offset:25088
	ds_read_b64_tr_b16 v[142:143], v192 offset:31232
	ds_read_b64_tr_b16 v[144:145], v192 offset:33280
	v_mfma_f32_32x32x16_bf16 v[32:47], v[88:91], v[222:225], v[32:47]
	v_mfma_f32_32x32x16_bf16 v[32:47], v[92:95], v[226:229], v[32:47]
	s_waitcnt lgkmcnt(0)
	v_mfma_f32_32x32x16_bf16 v[16:31], v[80:83], v[202:205], v[16:31]
	v_max_f32_e32 v80, v96, v97
	v_max3_f32 v81, v64, v65, v66
	v_max3_f32 v80, v80, v98, v99
	v_max3_f32 v81, v81, v67, v68
	v_max3_f32 v80, v80, v100, v101
	v_mfma_f32_32x32x16_bf16 v[16:31], v[84:87], v[206:209], v[16:31]
	v_max3_f32 v81, v81, v69, v70
	v_max3_f32 v80, v80, v102, v103
	v_max3_f32 v81, v81, v71, v72
	v_max3_f32 v80, v80, v104, v105
	v_max3_f32 v81, v81, v73, v74
	v_max3_f32 v80, v80, v106, v107
	v_max3_f32 v81, v81, v75, v76
	v_mfma_f32_32x32x16_bf16 v[16:31], v[88:91], v[138:141], v[16:31]
	v_max3_f32 v80, v80, v108, v109
	v_max3_f32 v81, v81, v77, v78
	v_max3_f32 v80, v80, v110, v111
	v_max3_f32 v80, v80, v81, v79
	v_mov_b32_e32 v197, 1.0
	v_mfma_f32_32x32x16_bf16 v[16:31], v[92:95], v[142:145], v[16:31]
	v_cmp_ge_f32_e64 s[0:1], s56, v80
	s_cmp_eq_u64 s[0:1], exec
	s_cbranch_scc1 .LBB0_799
	s_branch .LBB0_802

.LBB0_799:
	v_exp_f32_e32 v159, v96
	v_exp_f32_e32 v161, v97
	v_exp_f32_e32 v157, v98
	v_exp_f32_e32 v160, v99
	v_exp_f32_e32 v155, v100
	v_exp_f32_e32 v158, v101
	v_exp_f32_e32 v154, v102
	v_exp_f32_e32 v156, v103
	v_exp_f32_e32 v151, v104
	v_exp_f32_e32 v153, v105
	v_exp_f32_e32 v149, v106
	v_exp_f32_e32 v152, v107
	v_exp_f32_e32 v147, v108
	v_exp_f32_e32 v150, v109
	v_exp_f32_e32 v146, v110
	v_exp_f32_e32 v148, v111
	v_fma_f32 v80, v193, v179, v195
	v_fma_f32 v179, v80, v198, v199
	s_cmp_gt_u32 s55, 32
	s_waitcnt vmcnt(4) lgkmcnt(0)
	s_barrier
	s_cbranch_scc1 .LBB0_803
	s_add_i32 s55, s55, 2
	v_mov_b32_e32 v193, v197
	ds_read_b128 v[80:83], v130 offset:50176
	ds_read_b128 v[84:87], v130 offset:58368
	ds_read_b128 v[196:199], v131 offset:50176
	ds_read_b128 v[200:203], v131 offset:58368
	s_waitcnt lgkmcnt(2)
	v_mfma_f32_32x32x16_bf16 v[96:111], v[80:83], v[122:125], 0
	v_exp_f32_e32 v204, v72
	v_exp_f32_e32 v205, v73
	v_exp_f32_e32 v206, v74
	v_exp_f32_e32 v207, v75
	v_exp_f32_e32 v208, v76
	v_exp_f32_e32 v209, v77
	v_mfma_f32_32x32x16_bf16 v[80:95], v[84:87], v[122:125], 0
	v_exp_f32_e32 v210, v78
	v_exp_f32_e32 v79, v79
	s_waitcnt lgkmcnt(0)
	v_mfma_f32_32x32x16_bf16 v[96:111], v[196:199], v[126:129], v[96:111]
	v_mfma_f32_32x32x16_bf16 v[80:95], v[200:203], v[126:129], v[80:95]
	ds_read_b128 v[196:199], v132 offset:50176
	ds_read_b128 v[200:203], v132 offset:58368
	s_waitcnt lgkmcnt(0)
	v_mfma_f32_32x32x16_bf16 v[96:111], v[196:199], v[118:121], v[96:111]
	v_mfma_f32_32x32x16_bf16 v[80:95], v[200:203], v[118:121], v[80:95]
	ds_read_b128 v[196:199], v133 offset:50176
	ds_read_b128 v[200:203], v133 offset:58368
	v_exp_f32_e32 v180, v64
	v_add_f32_e32 v64, v161, v159
	v_add_f32_e32 v195, v157, v160
	v_add_f32_e32 v64, v155, v64
	v_add_f32_e32 v195, v158, v195
	v_add_f32_e32 v64, v154, v64
	v_add_f32_e32 v195, v156, v195
	v_add_f32_e32 v64, v151, v64
	v_add_f32_e32 v195, v153, v195
	v_add_f32_e32 v64, v149, v64
	v_add_f32_e32 v195, v152, v195
	v_add_f32_e32 v64, v147, v64
	s_waitcnt lgkmcnt(0)
	v_mfma_f32_32x32x16_bf16 v[96:111], v[196:199], v[114:117], v[96:111]
	v_exp_f32_e32 v197, v65
	v_add_f32_e32 v195, v150, v195
	v_exp_f32_e32 v198, v66
	v_add_f32_e32 v64, v146, v64
	v_exp_f32_e32 v199, v67
	v_add_f32_e32 v195, v148, v195
	v_add_f32_e32 v64, v180, v64
	v_mfma_f32_32x32x16_bf16 v[80:95], v[200:203], v[114:117], v[80:95]
	v_exp_f32_e32 v200, v68
	v_exp_f32_e32 v201, v69
	v_add_f32_e32 v195, v197, v195
	v_exp_f32_e32 v202, v70
	v_add_f32_e32 v64, v198, v64
	v_exp_f32_e32 v203, v71
	v_add_f32_e32 v195, v199, v195
	v_add_f32_e32 v64, v200, v64
	v_add_f32_e32 v195, v201, v195
	v_add_f32_e32 v64, v202, v64
	v_add_f32_e32 v195, v203, v195
	v_add_f32_e32 v64, v204, v64
	v_add_f32_e32 v195, v205, v195
	v_add_f32_e32 v64, v206, v64
	v_add_f32_e32 v195, v207, v195
	v_add_f32_e32 v64, v208, v64
	v_add_f32_e32 v195, v209, v195
	v_add_f32_e32 v64, v210, v64
	v_add_f32_e32 v195, v79, v195
	v_add_f32_e32 v195, v195, v64
	v_cvt_pk_bf16_f32 v64, v159, v161
	v_cvt_pk_bf16_f32 v65, v157, v160
	v_cvt_pk_bf16_f32 v66, v155, v158
	v_cvt_pk_bf16_f32 v67, v154, v156
	v_cvt_pk_bf16_f32 v68, v151, v153
	v_cvt_pk_bf16_f32 v69, v149, v152
	v_cvt_pk_bf16_f32 v70, v147, v150
	v_cvt_pk_bf16_f32 v71, v146, v148
	v_cvt_pk_bf16_f32 v72, v180, v197
	v_cvt_pk_bf16_f32 v73, v198, v199
	v_cvt_pk_bf16_f32 v74, v200, v201
	v_cvt_pk_bf16_f32 v75, v202, v203
	v_cvt_pk_bf16_f32 v76, v204, v205
	v_cvt_pk_bf16_f32 v77, v206, v207
	v_cvt_pk_bf16_f32 v78, v208, v209
	v_cvt_pk_bf16_f32 v79, v210, v79
	s_add_i32 m0, s84, 0x4400
	s_add_u32 s66, s78, s65
	s_addc_u32 s67, s79, 0
	global_load_lds_dwordx4 v185, s[66:67]
	s_add_i32 m0, s84, 0x6400
	s_add_i32 s64, s65, 0x60000
	global_load_lds_dwordx4 v184, s[66:67]
	s_add_i32 m0, s84, 0x14400
	s_add_u32 s70, s80, s64
	s_addc_u32 s71, s81, 0
	global_load_lds_dwordx4 v183, s[70:71]
	s_add_i32 m0, s84, 0x16400
	s_mov_b32 s65, s64
	global_load_lds_dwordx4 v182, s[70:71]
	ds_read_b64_tr_b16 v[198:199], v192 offset:33792
	ds_read_b64_tr_b16 v[200:201], v192 offset:35840
	ds_read_b64_tr_b16 v[202:203], v192 offset:37888
	ds_read_b64_tr_b16 v[204:205], v192 offset:39936
	ds_read_b64_tr_b16 v[206:207], v192 offset:41984
	ds_read_b64_tr_b16 v[208:209], v192 offset:44032
	ds_read_b64_tr_b16 v[222:223], v192 offset:46080
	ds_read_b64_tr_b16 v[224:225], v192 offset:48128
	s_waitcnt lgkmcnt(0)
	v_mfma_f32_32x32x16_bf16 v[0:15], v[64:67], v[198:201], v[0:15]
	ds_read_b64_tr_b16 v[198:199], v192 offset:34304
	ds_read_b64_tr_b16 v[200:201], v192 offset:36352
	ds_read_b64_tr_b16 v[138:139], v192 offset:42496
	ds_read_b64_tr_b16 v[140:141], v192 offset:44544
	v_mfma_f32_32x32x16_bf16 v[0:15], v[68:71], v[202:205], v[0:15]
	ds_read_b64_tr_b16 v[202:203], v192 offset:38400
	ds_read_b64_tr_b16 v[204:205], v192 offset:40448
	ds_read_b64_tr_b16 v[142:143], v192 offset:46592
	ds_read_b64_tr_b16 v[144:145], v192 offset:48640
	v_mfma_f32_32x32x16_bf16 v[0:15], v[72:75], v[206:209], v[0:15]
	v_mfma_f32_32x32x16_bf16 v[0:15], v[76:79], v[222:225], v[0:15]
	s_waitcnt lgkmcnt(0)
	v_mfma_f32_32x32x16_bf16 v[48:63], v[64:67], v[198:201], v[48:63]
	ds_read_b64_tr_b16 v[198:199], v192 offset:34816
	ds_read_b64_tr_b16 v[200:201], v192 offset:36864
	ds_read_b64_tr_b16 v[206:207], v192 offset:43008
	ds_read_b64_tr_b16 v[208:209], v192 offset:45056
	v_mfma_f32_32x32x16_bf16 v[48:63], v[68:71], v[202:205], v[48:63]
	ds_read_b64_tr_b16 v[202:203], v192 offset:38912
	ds_read_b64_tr_b16 v[204:205], v192 offset:40960
	ds_read_b64_tr_b16 v[222:223], v192 offset:47104
	ds_read_b64_tr_b16 v[224:225], v192 offset:49152
	v_mfma_f32_32x32x16_bf16 v[48:63], v[72:75], v[138:141], v[48:63]
	v_mfma_f32_32x32x16_bf16 v[48:63], v[76:79], v[142:145], v[48:63]
	s_waitcnt lgkmcnt(0)
	v_mfma_f32_32x32x16_bf16 v[32:47], v[64:67], v[198:201], v[32:47]
	ds_read_b64_tr_b16 v[198:199], v192 offset:35328
	ds_read_b64_tr_b16 v[200:201], v192 offset:37376
	ds_read_b64_tr_b16 v[138:139], v192 offset:43520
	ds_read_b64_tr_b16 v[140:141], v192 offset:45568
	v_mfma_f32_32x32x16_bf16 v[32:47], v[68:71], v[202:205], v[32:47]
	ds_read_b64_tr_b16 v[202:203], v192 offset:39424
	ds_read_b64_tr_b16 v[204:205], v192 offset:41472
	ds_read_b64_tr_b16 v[142:143], v192 offset:47616
	ds_read_b64_tr_b16 v[144:145], v192 offset:49664
	v_mfma_f32_32x32x16_bf16 v[32:47], v[72:75], v[206:209], v[32:47]
	v_mfma_f32_32x32x16_bf16 v[32:47], v[76:79], v[222:225], v[32:47]
	s_waitcnt lgkmcnt(0)
	v_mfma_f32_32x32x16_bf16 v[16:31], v[64:67], v[198:201], v[16:31]
	v_max_f32_e32 v64, v96, v97
	v_max3_f32 v65, v80, v81, v82
	v_max3_f32 v64, v64, v98, v99
	v_max3_f32 v65, v65, v83, v84
	v_max3_f32 v64, v64, v100, v101
	v_mfma_f32_32x32x16_bf16 v[16:31], v[68:71], v[202:205], v[16:31]
	v_max3_f32 v65, v65, v85, v86
	v_max3_f32 v64, v64, v102, v103
	v_max3_f32 v65, v65, v87, v88
	v_max3_f32 v64, v64, v104, v105
	v_max3_f32 v65, v65, v89, v90
	v_max3_f32 v64, v64, v106, v107
	v_max3_f32 v65, v65, v91, v92
	v_mfma_f32_32x32x16_bf16 v[16:31], v[72:75], v[138:141], v[16:31]
	v_max3_f32 v64, v64, v108, v109
	v_max3_f32 v65, v65, v93, v94
	v_max3_f32 v64, v64, v110, v111
	v_max3_f32 v64, v64, v65, v95
	v_mov_b32_e32 v198, 1.0
	v_mfma_f32_32x32x16_bf16 v[16:31], v[76:79], v[142:145], v[16:31]
	v_cmp_ge_f32_e64 s[0:1], s56, v64
	s_cmp_eq_u64 s[0:1], exec
	s_cbranch_scc1 .Lc1_792
	s_branch .Lc1_801

.Lc1_794:
	ds_read_b64_tr_b16 v[202:203], v192 offset:1024
	ds_read_b64_tr_b16 v[204:205], v192 offset:3072
	ds_read_b64_tr_b16 v[206:207], v192 offset:5120
	ds_read_b64_tr_b16 v[208:209], v192 offset:7168
	ds_read_b64_tr_b16 v[222:223], v192 offset:9216
	ds_read_b64_tr_b16 v[224:225], v192 offset:11264
	ds_read_b64_tr_b16 v[226:227], v192 offset:13312
	ds_read_b64_tr_b16 v[228:229], v192 offset:15360
	s_waitcnt lgkmcnt(0)
	v_mfma_f32_32x32x16_bf16 v[0:15], v[80:83], v[202:205], v[0:15]
	ds_read_b64_tr_b16 v[202:203], v192 offset:1536
	ds_read_b64_tr_b16 v[204:205], v192 offset:3584
	ds_read_b64_tr_b16 v[138:139], v192 offset:9728
	ds_read_b64_tr_b16 v[140:141], v192 offset:11776
	v_mfma_f32_32x32x16_bf16 v[0:15], v[84:87], v[206:209], v[0:15]
	ds_read_b64_tr_b16 v[206:207], v192 offset:5632
	ds_read_b64_tr_b16 v[208:209], v192 offset:7680
	ds_read_b64_tr_b16 v[142:143], v192 offset:13824
	ds_read_b64_tr_b16 v[144:145], v192 offset:15872
	v_mfma_f32_32x32x16_bf16 v[0:15], v[88:91], v[222:225], v[0:15]
	v_mfma_f32_32x32x16_bf16 v[0:15], v[92:95], v[226:229], v[0:15]
	s_waitcnt lgkmcnt(0)
	v_mfma_f32_32x32x16_bf16 v[48:63], v[80:83], v[202:205], v[48:63]
	ds_read_b64_tr_b16 v[202:203], v192 offset:2048
	ds_read_b64_tr_b16 v[204:205], v192 offset:4096
	ds_read_b64_tr_b16 v[222:223], v192 offset:10240
	ds_read_b64_tr_b16 v[224:225], v192 offset:12288
	v_mfma_f32_32x32x16_bf16 v[48:63], v[84:87], v[206:209], v[48:63]
	ds_read_b64_tr_b16 v[206:207], v192 offset:6144
	ds_read_b64_tr_b16 v[208:209], v192 offset:8192
	ds_read_b64_tr_b16 v[226:227], v192 offset:14336
	ds_read_b64_tr_b16 v[228:229], v192 offset:16384
	v_mfma_f32_32x32x16_bf16 v[48:63], v[88:91], v[138:141], v[48:63]
	v_mfma_f32_32x32x16_bf16 v[48:63], v[92:95], v[142:145], v[48:63]
	s_waitcnt lgkmcnt(0)
	v_mfma_f32_32x32x16_bf16 v[32:47], v[80:83], v[202:205], v[32:47]
	ds_read_b64_tr_b16 v[202:203], v192 offset:2560
	ds_read_b64_tr_b16 v[204:205], v192 offset:4608
	ds_read_b64_tr_b16 v[138:139], v192 offset:10752
	ds_read_b64_tr_b16 v[140:141], v192 offset:12800
	v_mfma_f32_32x32x16_bf16 v[32:47], v[84:87], v[206:209], v[32:47]
	ds_read_b64_tr_b16 v[206:207], v192 offset:6656
	ds_read_b64_tr_b16 v[208:209], v192 offset:8704
	ds_read_b64_tr_b16 v[142:143], v192 offset:14848
	ds_read_b64_tr_b16 v[144:145], v192 offset:16896
	v_mfma_f32_32x32x16_bf16 v[32:47], v[88:91], v[222:225], v[32:47]
	v_mfma_f32_32x32x16_bf16 v[32:47], v[92:95], v[226:229], v[32:47]
	s_waitcnt lgkmcnt(0)
	v_mfma_f32_32x32x16_bf16 v[16:31], v[80:83], v[202:205], v[16:31]
	v_max_f32_e32 v80, v96, v97
	v_max3_f32 v81, v64, v65, v66
	v_max3_f32 v80, v80, v98, v99
	v_max3_f32 v81, v81, v67, v68
	v_max3_f32 v80, v80, v100, v101
	v_mfma_f32_32x32x16_bf16 v[16:31], v[84:87], v[206:209], v[16:31]
	v_max3_f32 v81, v81, v69, v70
	v_max3_f32 v80, v80, v102, v103
	v_max3_f32 v81, v81, v71, v72
	v_max3_f32 v80, v80, v104, v105
	v_max3_f32 v81, v81, v73, v74
	v_max3_f32 v80, v80, v106, v107
	v_max3_f32 v81, v81, v75, v76
	v_mfma_f32_32x32x16_bf16 v[16:31], v[88:91], v[138:141], v[16:31]
	v_max3_f32 v80, v80, v108, v109
	v_max3_f32 v81, v81, v77, v78
	v_max3_f32 v80, v80, v110, v111
	v_max3_f32 v80, v80, v81, v79
	v_mov_b32_e32 v197, 1.0
	v_mfma_f32_32x32x16_bf16 v[16:31], v[92:95], v[142:145], v[16:31]
	v_cmp_ge_f32_e64 s[0:1], s56, v80
	s_cmp_eq_u64 s[0:1], exec
	s_cbranch_scc1 .Lc1_799
	s_branch .Lc1_802

.Lc1_799:
	v_exp_f32_e32 v159, v96
	v_exp_f32_e32 v161, v97
	v_exp_f32_e32 v157, v98
	v_exp_f32_e32 v160, v99
	v_exp_f32_e32 v155, v100
	v_exp_f32_e32 v158, v101
	v_exp_f32_e32 v154, v102
	v_exp_f32_e32 v156, v103
	v_exp_f32_e32 v151, v104
	v_exp_f32_e32 v153, v105
	v_exp_f32_e32 v149, v106
	v_exp_f32_e32 v152, v107
	v_exp_f32_e32 v147, v108
	v_exp_f32_e32 v150, v109
	v_exp_f32_e32 v146, v110
	v_exp_f32_e32 v148, v111
	v_fma_f32 v80, v193, v179, v195
	v_fma_f32 v179, v80, v198, v199
	s_cmp_gt_u32 s55, 32
	s_waitcnt vmcnt(4) lgkmcnt(0)
	s_barrier
	s_cbranch_scc1 .LBB0_803
	s_add_i32 s55, s55, 2
	v_mov_b32_e32 v193, v197
	ds_read_b128 v[80:83], v134 offset:50176
	ds_read_b128 v[84:87], v134 offset:58368
	ds_read_b128 v[196:199], v135 offset:50176
	ds_read_b128 v[200:203], v135 offset:58368
	s_waitcnt lgkmcnt(2)
	v_mfma_f32_32x32x16_bf16 v[96:111], v[80:83], v[122:125], 0
	v_exp_f32_e32 v204, v72
	v_exp_f32_e32 v205, v73
	v_exp_f32_e32 v206, v74
	v_exp_f32_e32 v207, v75
	v_exp_f32_e32 v208, v76
	v_exp_f32_e32 v209, v77
	v_mfma_f32_32x32x16_bf16 v[80:95], v[84:87], v[122:125], 0
	v_exp_f32_e32 v210, v78
	v_exp_f32_e32 v79, v79
	s_waitcnt lgkmcnt(0)
	v_mfma_f32_32x32x16_bf16 v[96:111], v[196:199], v[126:129], v[96:111]
	v_mfma_f32_32x32x16_bf16 v[80:95], v[200:203], v[126:129], v[80:95]
	ds_read_b128 v[196:199], v136 offset:50176
	ds_read_b128 v[200:203], v136 offset:58368
	s_waitcnt lgkmcnt(0)
	v_mfma_f32_32x32x16_bf16 v[96:111], v[196:199], v[118:121], v[96:111]
	v_mfma_f32_32x32x16_bf16 v[80:95], v[200:203], v[118:121], v[80:95]
	ds_read_b128 v[196:199], v137 offset:50176
	ds_read_b128 v[200:203], v137 offset:58368
	v_exp_f32_e32 v180, v64
	v_add_f32_e32 v64, v161, v159
	v_add_f32_e32 v195, v157, v160
	v_add_f32_e32 v64, v155, v64
	v_add_f32_e32 v195, v158, v195
	v_add_f32_e32 v64, v154, v64
	v_add_f32_e32 v195, v156, v195
	v_add_f32_e32 v64, v151, v64
	v_add_f32_e32 v195, v153, v195
	v_add_f32_e32 v64, v149, v64
	v_add_f32_e32 v195, v152, v195
	v_add_f32_e32 v64, v147, v64
	s_waitcnt lgkmcnt(0)
	v_mfma_f32_32x32x16_bf16 v[96:111], v[196:199], v[114:117], v[96:111]
	v_exp_f32_e32 v197, v65
	v_add_f32_e32 v195, v150, v195
	v_exp_f32_e32 v198, v66
	v_add_f32_e32 v64, v146, v64
	v_exp_f32_e32 v199, v67
	v_add_f32_e32 v195, v148, v195
	v_add_f32_e32 v64, v180, v64
	v_mfma_f32_32x32x16_bf16 v[80:95], v[200:203], v[114:117], v[80:95]
	v_exp_f32_e32 v200, v68
	v_exp_f32_e32 v201, v69
	v_add_f32_e32 v195, v197, v195
	v_exp_f32_e32 v202, v70
	v_add_f32_e32 v64, v198, v64
	v_exp_f32_e32 v203, v71
	v_add_f32_e32 v195, v199, v195
	v_add_f32_e32 v64, v200, v64
	v_add_f32_e32 v195, v201, v195
	v_add_f32_e32 v64, v202, v64
	v_add_f32_e32 v195, v203, v195
	v_add_f32_e32 v64, v204, v64
	v_add_f32_e32 v195, v205, v195
	v_add_f32_e32 v64, v206, v64
	v_add_f32_e32 v195, v207, v195
	v_add_f32_e32 v64, v208, v64
	v_add_f32_e32 v195, v209, v195
	v_add_f32_e32 v64, v210, v64
	v_add_f32_e32 v195, v79, v195
	v_add_f32_e32 v195, v195, v64
	v_cvt_pk_bf16_f32 v64, v159, v161
	v_cvt_pk_bf16_f32 v65, v157, v160
	v_cvt_pk_bf16_f32 v66, v155, v158
	v_cvt_pk_bf16_f32 v67, v154, v156
	v_cvt_pk_bf16_f32 v68, v151, v153
	v_cvt_pk_bf16_f32 v69, v149, v152
	v_cvt_pk_bf16_f32 v70, v147, v150
	v_cvt_pk_bf16_f32 v71, v146, v148
	v_cvt_pk_bf16_f32 v72, v180, v197
	v_cvt_pk_bf16_f32 v73, v198, v199
	v_cvt_pk_bf16_f32 v74, v200, v201
	v_cvt_pk_bf16_f32 v75, v202, v203
	v_cvt_pk_bf16_f32 v76, v204, v205
	v_cvt_pk_bf16_f32 v77, v206, v207
	v_cvt_pk_bf16_f32 v78, v208, v209
	v_cvt_pk_bf16_f32 v79, v210, v79
	s_add_i32 m0, s84, 0x400
	s_add_u32 s66, s78, s65
	s_addc_u32 s67, s79, 0
	global_load_lds_dwordx4 v185, s[66:67]
	s_add_i32 m0, s84, 0x2400
	s_add_i32 s64, s65, 0x60000
	global_load_lds_dwordx4 v184, s[66:67]
	s_add_i32 m0, s84, 0x10400
	s_add_u32 s70, s80, s64
	s_addc_u32 s71, s81, 0
	global_load_lds_dwordx4 v183, s[70:71]
	s_add_i32 m0, s84, 0x12400
	s_mov_b32 s65, s64
	global_load_lds_dwordx4 v182, s[70:71]
	ds_read_b64_tr_b16 v[198:199], v192 offset:17408
	ds_read_b64_tr_b16 v[200:201], v192 offset:19456
	ds_read_b64_tr_b16 v[202:203], v192 offset:21504
	ds_read_b64_tr_b16 v[204:205], v192 offset:23552
	ds_read_b64_tr_b16 v[206:207], v192 offset:25600
	ds_read_b64_tr_b16 v[208:209], v192 offset:27648
	ds_read_b64_tr_b16 v[222:223], v192 offset:29696
	ds_read_b64_tr_b16 v[224:225], v192 offset:31744
	s_waitcnt lgkmcnt(0)
	v_mfma_f32_32x32x16_bf16 v[0:15], v[64:67], v[198:201], v[0:15]
	ds_read_b64_tr_b16 v[198:199], v192 offset:17920
	ds_read_b64_tr_b16 v[200:201], v192 offset:19968
	ds_read_b64_tr_b16 v[138:139], v192 offset:26112
	ds_read_b64_tr_b16 v[140:141], v192 offset:28160
	v_mfma_f32_32x32x16_bf16 v[0:15], v[68:71], v[202:205], v[0:15]
	ds_read_b64_tr_b16 v[202:203], v192 offset:22016
	ds_read_b64_tr_b16 v[204:205], v192 offset:24064
	ds_read_b64_tr_b16 v[142:143], v192 offset:30208
	ds_read_b64_tr_b16 v[144:145], v192 offset:32256
	v_mfma_f32_32x32x16_bf16 v[0:15], v[72:75], v[206:209], v[0:15]
	v_mfma_f32_32x32x16_bf16 v[0:15], v[76:79], v[222:225], v[0:15]
	s_waitcnt lgkmcnt(0)
	v_mfma_f32_32x32x16_bf16 v[48:63], v[64:67], v[198:201], v[48:63]
	ds_read_b64_tr_b16 v[198:199], v192 offset:18432
	ds_read_b64_tr_b16 v[200:201], v192 offset:20480
	ds_read_b64_tr_b16 v[206:207], v192 offset:26624
	ds_read_b64_tr_b16 v[208:209], v192 offset:28672
	v_mfma_f32_32x32x16_bf16 v[48:63], v[68:71], v[202:205], v[48:63]
	ds_read_b64_tr_b16 v[202:203], v192 offset:22528
	ds_read_b64_tr_b16 v[204:205], v192 offset:24576
	ds_read_b64_tr_b16 v[222:223], v192 offset:30720
	ds_read_b64_tr_b16 v[224:225], v192 offset:32768
	v_mfma_f32_32x32x16_bf16 v[48:63], v[72:75], v[138:141], v[48:63]
	v_mfma_f32_32x32x16_bf16 v[48:63], v[76:79], v[142:145], v[48:63]
	s_waitcnt lgkmcnt(0)
	v_mfma_f32_32x32x16_bf16 v[32:47], v[64:67], v[198:201], v[32:47]
	ds_read_b64_tr_b16 v[198:199], v192 offset:18944
	ds_read_b64_tr_b16 v[200:201], v192 offset:20992
	ds_read_b64_tr_b16 v[138:139], v192 offset:27136
	ds_read_b64_tr_b16 v[140:141], v192 offset:29184
	v_mfma_f32_32x32x16_bf16 v[32:47], v[68:71], v[202:205], v[32:47]
	ds_read_b64_tr_b16 v[202:203], v192 offset:23040
	ds_read_b64_tr_b16 v[204:205], v192 offset:25088
	ds_read_b64_tr_b16 v[142:143], v192 offset:31232
	ds_read_b64_tr_b16 v[144:145], v192 offset:33280
	v_mfma_f32_32x32x16_bf16 v[32:47], v[72:75], v[206:209], v[32:47]
	v_mfma_f32_32x32x16_bf16 v[32:47], v[76:79], v[222:225], v[32:47]
	s_waitcnt lgkmcnt(0)
	v_mfma_f32_32x32x16_bf16 v[16:31], v[64:67], v[198:201], v[16:31]
	v_max_f32_e32 v64, v96, v97
	v_max3_f32 v65, v80, v81, v82
	v_max3_f32 v64, v64, v98, v99
	v_max3_f32 v65, v65, v83, v84
	v_max3_f32 v64, v64, v100, v101
	v_mfma_f32_32x32x16_bf16 v[16:31], v[68:71], v[202:205], v[16:31]
	v_max3_f32 v65, v65, v85, v86
	v_max3_f32 v64, v64, v102, v103
	v_max3_f32 v65, v65, v87, v88
	v_max3_f32 v64, v64, v104, v105
	v_max3_f32 v65, v65, v89, v90
	v_max3_f32 v64, v64, v106, v107
	v_max3_f32 v65, v65, v91, v92
	v_mfma_f32_32x32x16_bf16 v[16:31], v[72:75], v[138:141], v[16:31]
	v_max3_f32 v64, v64, v108, v109
	v_max3_f32 v65, v65, v93, v94
	v_max3_f32 v64, v64, v110, v111
	v_max3_f32 v64, v64, v65, v95
	v_mov_b32_e32 v198, 1.0
	v_mfma_f32_32x32x16_bf16 v[16:31], v[76:79], v[142:145], v[16:31]
	v_cmp_ge_f32_e64 s[0:1], s56, v64
	s_cmp_eq_u64 s[0:1], exec
	s_cbranch_scc1 .Lc2_792
	s_branch .Lc2_801

.Lc2_794:
	ds_read_b64_tr_b16 v[202:203], v192 offset:33792
	ds_read_b64_tr_b16 v[204:205], v192 offset:35840
	ds_read_b64_tr_b16 v[206:207], v192 offset:37888
	ds_read_b64_tr_b16 v[208:209], v192 offset:39936
	ds_read_b64_tr_b16 v[222:223], v192 offset:41984
	ds_read_b64_tr_b16 v[224:225], v192 offset:44032
	ds_read_b64_tr_b16 v[226:227], v192 offset:46080
	ds_read_b64_tr_b16 v[228:229], v192 offset:48128
	s_waitcnt lgkmcnt(0)
	v_mfma_f32_32x32x16_bf16 v[0:15], v[80:83], v[202:205], v[0:15]
	ds_read_b64_tr_b16 v[202:203], v192 offset:34304
	ds_read_b64_tr_b16 v[204:205], v192 offset:36352
	ds_read_b64_tr_b16 v[138:139], v192 offset:42496
	ds_read_b64_tr_b16 v[140:141], v192 offset:44544
	v_mfma_f32_32x32x16_bf16 v[0:15], v[84:87], v[206:209], v[0:15]
	ds_read_b64_tr_b16 v[206:207], v192 offset:38400
	ds_read_b64_tr_b16 v[208:209], v192 offset:40448
	ds_read_b64_tr_b16 v[142:143], v192 offset:46592
	ds_read_b64_tr_b16 v[144:145], v192 offset:48640
	v_mfma_f32_32x32x16_bf16 v[0:15], v[88:91], v[222:225], v[0:15]
	v_mfma_f32_32x32x16_bf16 v[0:15], v[92:95], v[226:229], v[0:15]
	s_waitcnt lgkmcnt(0)
	v_mfma_f32_32x32x16_bf16 v[48:63], v[80:83], v[202:205], v[48:63]
	ds_read_b64_tr_b16 v[202:203], v192 offset:34816
	ds_read_b64_tr_b16 v[204:205], v192 offset:36864
	ds_read_b64_tr_b16 v[222:223], v192 offset:43008
	ds_read_b64_tr_b16 v[224:225], v192 offset:45056
	v_mfma_f32_32x32x16_bf16 v[48:63], v[84:87], v[206:209], v[48:63]
	ds_read_b64_tr_b16 v[206:207], v192 offset:38912
	ds_read_b64_tr_b16 v[208:209], v192 offset:40960
	ds_read_b64_tr_b16 v[226:227], v192 offset:47104
	ds_read_b64_tr_b16 v[228:229], v192 offset:49152
	v_mfma_f32_32x32x16_bf16 v[48:63], v[88:91], v[138:141], v[48:63]
	v_mfma_f32_32x32x16_bf16 v[48:63], v[92:95], v[142:145], v[48:63]
	s_waitcnt lgkmcnt(0)
	v_mfma_f32_32x32x16_bf16 v[32:47], v[80:83], v[202:205], v[32:47]
	ds_read_b64_tr_b16 v[202:203], v192 offset:35328
	ds_read_b64_tr_b16 v[204:205], v192 offset:37376
	ds_read_b64_tr_b16 v[138:139], v192 offset:43520
	ds_read_b64_tr_b16 v[140:141], v192 offset:45568
	v_mfma_f32_32x32x16_bf16 v[32:47], v[84:87], v[206:209], v[32:47]
	ds_read_b64_tr_b16 v[206:207], v192 offset:39424
	ds_read_b64_tr_b16 v[208:209], v192 offset:41472
	ds_read_b64_tr_b16 v[142:143], v192 offset:47616
	ds_read_b64_tr_b16 v[144:145], v192 offset:49664
	v_mfma_f32_32x32x16_bf16 v[32:47], v[88:91], v[222:225], v[32:47]
	v_mfma_f32_32x32x16_bf16 v[32:47], v[92:95], v[226:229], v[32:47]
	s_waitcnt lgkmcnt(0)
	v_mfma_f32_32x32x16_bf16 v[16:31], v[80:83], v[202:205], v[16:31]
	v_max_f32_e32 v80, v96, v97
	v_max3_f32 v81, v64, v65, v66
	v_max3_f32 v80, v80, v98, v99
	v_max3_f32 v81, v81, v67, v68
	v_max3_f32 v80, v80, v100, v101
	v_mfma_f32_32x32x16_bf16 v[16:31], v[84:87], v[206:209], v[16:31]
	v_max3_f32 v81, v81, v69, v70
	v_max3_f32 v80, v80, v102, v103
	v_max3_f32 v81, v81, v71, v72
	v_max3_f32 v80, v80, v104, v105
	v_max3_f32 v81, v81, v73, v74
	v_max3_f32 v80, v80, v106, v107
	v_max3_f32 v81, v81, v75, v76
	v_mfma_f32_32x32x16_bf16 v[16:31], v[88:91], v[138:141], v[16:31]
	v_max3_f32 v80, v80, v108, v109
	v_max3_f32 v81, v81, v77, v78
	v_max3_f32 v80, v80, v110, v111
	v_max3_f32 v80, v80, v81, v79
	v_mov_b32_e32 v197, 1.0
	v_mfma_f32_32x32x16_bf16 v[16:31], v[92:95], v[142:145], v[16:31]
	v_cmp_ge_f32_e64 s[0:1], s56, v80
	s_cmp_eq_u64 s[0:1], exec
	s_cbranch_scc1 .Lc2_799
	s_branch .Lc2_802
